# O(1) unit lookup in the gate/up loop: a per-expert cumulative tile table in one VGPR, searched with one v_cmp + s_bcnt1, replaces the 32-way unrolled scalar walk with its integer division
# speedup vs baseline: 1.0075x; 1.0049x over previous
; __device__ __forceinline__ int tid_opaque() { int t = threadIdx.x; asm volatile("" : "+v"(t)); return t; }
; __device__ __forceinline__ int vwg_id() { const int G = gridDim.x; return (G % 8 == 0) ? (int)((blockIdx.x % 8) * (G / 8) + blockIdx.x / 8) : (int)blockIdx.x; }
; __device__ __forceinline__ bool moe_unit(int cv, int u, int ntiles_n, MoeUnit& mu) {
;     int base = 0;
; #pragma unroll
;     for (int e = 0; e < E; ++e) { const int c = __builtin_amdgcn_readlane(cv, e), tm = (c + 255) >> 8, nu = tm * ntiles_n;
;         if (u < nu) { mu.e = e; mu.cnt = c; mu.base = base; mu.nt = u / tm; mu.mt = u - mu.nt * tm; mu.light = (mu.mt == tm - 1 && c - mu.mt * 256 <= 128) ? 1 : 0; return true; }
;         u -= nu; base += tm * 256; }
;     return false;
; }
; __device__ __forceinline__ void phase_moe_gu(const Ptrs& p, LAS unsigned char* lds) {
;     ...
;     MoeUnit mu; const int cv = counts[tid_opaque() & 31];
;     for (int u = vwg_id(); moe_unit(cv, u, 16, mu); u += gridDim.x) {
.LBB0_1003:
	s_add_u32 s20, s30, 0x18248000
	s_addc_u32 s28, s31, 0
	s_and_b32 s21, s28, 0xffff
	s_mov_b32 s27, 0x20000
	s_mov_b32 s26, 0x7ffffff0
	s_and_b32 s37, s37, 0xffff
	s_movk_i32 s66, 0x6000
	s_mov_b32 s67, 0x80000
	s_mov_b32 s76, 0x82000
	s_mov_b32 s77, 0x84000
	s_mov_b32 s78, 0x86000
	s_mov_b32 s79, 0x88000
	s_mov_b32 s80, 0x8a000
	s_mov_b32 s81, 0x8c000
	s_mov_b32 s82, 0x8e000
	s_movk_i32 s83, 0xf80
	s_add_i32 s29, 0, 0x18000
	s_add_i32 s64, 0, 0x10400
	s_mov_b32 s84, 0xc0e00000
	v_mov_b32_e32 v2, 0
	v_mov_b32_e32 v214, 0x40e00000
	s_waitcnt vmcnt(0)
	v_mov_b32_e32 v247, 0x7fffffff
	s_mov_b32 s1, 0
	v_readlane_b32 s2, v1, 0
	s_add_i32 s2, s2, 0xff
	s_ashr_i32 s2, s2, 8
	s_add_i32 s1, s1, s2
	v_writelane_b32 v247, s1, 0
	v_readlane_b32 s2, v1, 1
	s_add_i32 s2, s2, 0xff
	s_ashr_i32 s2, s2, 8
	s_add_i32 s1, s1, s2
	v_writelane_b32 v247, s1, 1
	v_readlane_b32 s2, v1, 2
	s_add_i32 s2, s2, 0xff
	s_ashr_i32 s2, s2, 8
	s_add_i32 s1, s1, s2
	v_writelane_b32 v247, s1, 2
	v_readlane_b32 s2, v1, 3
	s_add_i32 s2, s2, 0xff
	s_ashr_i32 s2, s2, 8
	s_add_i32 s1, s1, s2
	v_writelane_b32 v247, s1, 3
	v_readlane_b32 s2, v1, 4
	s_add_i32 s2, s2, 0xff
	s_ashr_i32 s2, s2, 8
	s_add_i32 s1, s1, s2
	v_writelane_b32 v247, s1, 4
	v_readlane_b32 s2, v1, 5
	s_add_i32 s2, s2, 0xff
	s_ashr_i32 s2, s2, 8
	s_add_i32 s1, s1, s2
	v_writelane_b32 v247, s1, 5
	v_readlane_b32 s2, v1, 6
	s_add_i32 s2, s2, 0xff
	s_ashr_i32 s2, s2, 8
	s_add_i32 s1, s1, s2
	v_writelane_b32 v247, s1, 6
	v_readlane_b32 s2, v1, 7
	s_add_i32 s2, s2, 0xff
	s_ashr_i32 s2, s2, 8
	s_add_i32 s1, s1, s2
	v_writelane_b32 v247, s1, 7
	v_readlane_b32 s2, v1, 8
	s_add_i32 s2, s2, 0xff
	s_ashr_i32 s2, s2, 8
	s_add_i32 s1, s1, s2
	v_writelane_b32 v247, s1, 8
	v_readlane_b32 s2, v1, 9
	s_add_i32 s2, s2, 0xff
	s_ashr_i32 s2, s2, 8
	s_add_i32 s1, s1, s2
	v_writelane_b32 v247, s1, 9
	v_readlane_b32 s2, v1, 10
	s_add_i32 s2, s2, 0xff
	s_ashr_i32 s2, s2, 8
	s_add_i32 s1, s1, s2
	v_writelane_b32 v247, s1, 10
	v_readlane_b32 s2, v1, 11
	s_add_i32 s2, s2, 0xff
	s_ashr_i32 s2, s2, 8
	s_add_i32 s1, s1, s2
	v_writelane_b32 v247, s1, 11
	v_readlane_b32 s2, v1, 12
	s_add_i32 s2, s2, 0xff
	s_ashr_i32 s2, s2, 8
	s_add_i32 s1, s1, s2
	v_writelane_b32 v247, s1, 12
	v_readlane_b32 s2, v1, 13
	s_add_i32 s2, s2, 0xff
	s_ashr_i32 s2, s2, 8
	s_add_i32 s1, s1, s2
	v_writelane_b32 v247, s1, 13
	v_readlane_b32 s2, v1, 14
	s_add_i32 s2, s2, 0xff
	s_ashr_i32 s2, s2, 8
	s_add_i32 s1, s1, s2
	v_writelane_b32 v247, s1, 14
	v_readlane_b32 s2, v1, 15
	s_add_i32 s2, s2, 0xff
	s_ashr_i32 s2, s2, 8
	s_add_i32 s1, s1, s2
	v_writelane_b32 v247, s1, 15
	v_readlane_b32 s2, v1, 16
	s_add_i32 s2, s2, 0xff
	s_ashr_i32 s2, s2, 8
	s_add_i32 s1, s1, s2
	v_writelane_b32 v247, s1, 16
	v_readlane_b32 s2, v1, 17
	s_add_i32 s2, s2, 0xff
	s_ashr_i32 s2, s2, 8
	s_add_i32 s1, s1, s2
	v_writelane_b32 v247, s1, 17
	v_readlane_b32 s2, v1, 18
	s_add_i32 s2, s2, 0xff
	s_ashr_i32 s2, s2, 8
	s_add_i32 s1, s1, s2
	v_writelane_b32 v247, s1, 18
	v_readlane_b32 s2, v1, 19
	s_add_i32 s2, s2, 0xff
	s_ashr_i32 s2, s2, 8
	s_add_i32 s1, s1, s2
	v_writelane_b32 v247, s1, 19
	v_readlane_b32 s2, v1, 20
	s_add_i32 s2, s2, 0xff
	s_ashr_i32 s2, s2, 8
	s_add_i32 s1, s1, s2
	v_writelane_b32 v247, s1, 20
	v_readlane_b32 s2, v1, 21
	s_add_i32 s2, s2, 0xff
	s_ashr_i32 s2, s2, 8
	s_add_i32 s1, s1, s2
	v_writelane_b32 v247, s1, 21
	v_readlane_b32 s2, v1, 22
	s_add_i32 s2, s2, 0xff
	s_ashr_i32 s2, s2, 8
	s_add_i32 s1, s1, s2
	v_writelane_b32 v247, s1, 22
	v_readlane_b32 s2, v1, 23
	s_add_i32 s2, s2, 0xff
	s_ashr_i32 s2, s2, 8
	s_add_i32 s1, s1, s2
	v_writelane_b32 v247, s1, 23
	v_readlane_b32 s2, v1, 24
	s_add_i32 s2, s2, 0xff
	s_ashr_i32 s2, s2, 8
	s_add_i32 s1, s1, s2
	v_writelane_b32 v247, s1, 24
	v_readlane_b32 s2, v1, 25
	s_add_i32 s2, s2, 0xff
	s_ashr_i32 s2, s2, 8
	s_add_i32 s1, s1, s2
	v_writelane_b32 v247, s1, 25
	v_readlane_b32 s2, v1, 26
	s_add_i32 s2, s2, 0xff
	s_ashr_i32 s2, s2, 8
	s_add_i32 s1, s1, s2
	v_writelane_b32 v247, s1, 26
	v_readlane_b32 s2, v1, 27
	s_add_i32 s2, s2, 0xff
	s_ashr_i32 s2, s2, 8
	s_add_i32 s1, s1, s2
	v_writelane_b32 v247, s1, 27
	v_readlane_b32 s2, v1, 28
	s_add_i32 s2, s2, 0xff
	s_ashr_i32 s2, s2, 8
	s_add_i32 s1, s1, s2
	v_writelane_b32 v247, s1, 28
	v_readlane_b32 s2, v1, 29
	s_add_i32 s2, s2, 0xff
	s_ashr_i32 s2, s2, 8
	s_add_i32 s1, s1, s2
	v_writelane_b32 v247, s1, 29
	v_readlane_b32 s2, v1, 30
	s_add_i32 s2, s2, 0xff
	s_ashr_i32 s2, s2, 8
	s_add_i32 s1, s1, s2
	v_writelane_b32 v247, s1, 30
	v_readlane_b32 s2, v1, 31
	s_add_i32 s2, s2, 0xff
	s_ashr_i32 s2, s2, 8
	s_add_i32 s1, s1, s2
	v_writelane_b32 v247, s1, 31
	s_branch .LBB0_1006

; __device__ __forceinline__ __amdgpu_buffer_rsrc_t mk_rsrc(const void* p) { return __builtin_amdgcn_make_buffer_rsrc((void*)p, 0, 0x7ffffff0, 0x00020000); }
; __device__ __forceinline__ int vwg_id() { const int G = gridDim.x; return (G % 8 == 0) ? (int)((blockIdx.x % 8) * (G / 8) + blockIdx.x / 8) : (int)blockIdx.x; }
; __device__ __forceinline__ bool moe_unit(int cv, int u, int ntiles_n, MoeUnit& mu) {
;     int base = 0;
; #pragma unroll
;     for (int e = 0; e < E; ++e) { const int c = __builtin_amdgcn_readlane(cv, e), tm = (c + 255) >> 8, nu = tm * ntiles_n;
;         if (u < nu) { mu.e = e; mu.cnt = c; mu.base = base; mu.nt = u / tm; mu.mt = u - mu.nt * tm; mu.light = (mu.mt == tm - 1 && c - mu.mt * 256 <= 128) ? 1 : 0; return true; }
;         u -= nu; base += tm * 256; }
;     return false;
; }
; __device__ __forceinline__ void phase_moe_gu(const Ptrs& p, LAS unsigned char* lds) {
;     ...
;     for (int u = vwg_id(); moe_unit(cv, u, 16, mu); u += gridDim.x) {
;         GemmT T; T.init();
;         const int* list = (const int*)(p.ws + OFF_LIST) + (size_t)mu.e * NTOK; const int i0 = mu.mt * 256, n0 = mu.nt * 128;
;         unsigned ao[4];
; #pragma unroll
;         for (int i = 0; i < 4; ++i) { const int r = i0 + T.aR + 64 * i; const int tok = (r < mu.cnt) ? (list[r] >> 2) : 0; ao[i] = (unsigned)((tok * D + T.aC) * 2); }
;         const float* wsel = ((__builtin_amdgcn_readfirstlane(T.b_p) & 1) ? p.w_up : p.w_gate) + (size_t)mu.e * D * D + n0;
;         const unsigned bo = (unsigned)((T.b_k * D + T.b_gucol) * 4);
;         f32x4 acc[8][4]; acc_zero(acc);
;         const int mlim = __builtin_amdgcn_readfirstlane(T.wr) ? 0 : ((mu.cnt - i0 + 15) >> 4);
;         if (mu.light) gemm_kloop_light(acc, lds, T, mk_rsrc(h2), ao[0], ao[1], ao[2], ao[3], mk_rsrc(wsel), bo, D * 4u, D / 64, mlim);
;         else gemm_kloop(acc, lds, T, mk_rsrc(h2), ao[0], ao[1], ao[2], ao[3], mk_rsrc(wsel), bo, D * 4u, D / 64);
.LBB0_1006:
	s_waitcnt vmcnt(0)
	s_lshr_b32 s2, s65, 4
	v_cmp_ge_i32_e32 vcc, s2, v247
	s_bcnt1_i32_b64 s42, vcc
	s_cmp_ge_u32 s42, 32
	s_cbranch_scc1 .LBB0_1288
	s_nop 1
	v_readlane_b32 s87, v1, s42
	v_readlane_b32 s4, v247, s42
	s_add_i32 s3, s87, 0xff
	s_ashr_i32 s3, s3, 8
	s_sub_i32 s4, s4, s3
	s_lshl_b32 s88, s4, 8
	s_lshl_b32 s4, s4, 4
	s_sub_i32 s2, s65, s4
	s_mov_b32 s85, 0
.Lmy_wk_m:
	s_cmp_lt_i32 s2, s3
	s_cbranch_scc1 .Lmy_wk_d
	s_sub_i32 s2, s2, s3
	s_add_i32 s85, s85, 1
	s_branch .Lmy_wk_m
.Lmy_wk_d:
	s_mov_b32 s86, s2
	s_add_i32 s4, s3, -1
	s_cmp_eq_u32 s86, s4
	s_cselect_b64 s[0:1], -1, 0
	s_lshl_b32 s4, s86, 8
	s_sub_i32 s4, s87, s4
	s_cmpk_lt_i32 s4, 0x81
	s_cselect_b64 s[4:5], -1, 0
	s_and_b64 s[0:1], s[0:1], s[4:5]
	v_cndmask_b32_e64 v215, 0, 1, s[0:1]
	s_ashr_i32 s43, s42, 31
	s_lshl_b64 s[0:1], s[42:43], 15
	v_mov_b32_e32 v3, v0
	s_add_u32 s0, s52, s0
	s_addc_u32 s1, s53, s1
	v_bfe_u32 v4, v3, 2, 4
	s_lshl_b32 s2, s86, 8
	v_ashrrev_i32_e32 v10, 7, v3
	v_or_b32_e32 v4, s2, v4
	v_lshl_add_u32 v4, v10, 4, v4
	v_cmp_gt_i32_e32 vcc, s87, v4
	v_mov_b32_e32 v6, 0
	v_ashrrev_i32_e32 v5, 31, v4
	v_mov_b32_e32 v7, 0
	v_mov_b32_e32 v8, 0
	v_mov_b32_e32 v9, 0
	v_lshl_add_u64 v[12:13], v[4:5], 2, s[0:1]
	s_and_saveexec_b64 s[4:5], vcc
	global_load_dword v7, v[12:13], off
	s_or_b64 exec, exec, s[4:5]
	v_add_u32_e32 v11, 64, v4
	v_cmp_gt_i32_e32 vcc, s87, v11
	s_and_saveexec_b64 s[4:5], vcc
	global_load_dword v6, v[12:13], off offset:256
	s_or_b64 exec, exec, s[4:5]
	v_add_u32_e32 v11, 0x80, v4
	v_cmp_gt_i32_e32 vcc, s87, v11
	s_and_saveexec_b64 s[4:5], vcc
	global_load_dword v9, v[12:13], off offset:512
	s_or_b64 exec, exec, s[4:5]
	v_add_u32_e32 v11, 0xc0, v4
	v_cmp_gt_i32_e32 vcc, s87, v11
	s_and_saveexec_b64 s[4:5], vcc
	global_load_dword v8, v[12:13], off offset:768
	s_or_b64 exec, exec, s[4:5]
	v_ashrrev_i32_e32 v5, 6, v3
	v_and_b32_e32 v11, 1, v5
	s_lshl_b32 s0, s85, 7
	v_readfirstlane_b32 s1, v11
	v_readlane_b32 s4, v246, 0
	s_bitcmp0_b32 s1, 0
	v_readlane_b32 s5, v246, 1
	s_cselect_b32 s1, s49, s5
	s_cselect_b32 s3, s48, s4
	s_lshl_b64 s[4:5], s[42:43], 24
	v_readlane_b32 s6, v246, 2
	s_add_u32 s3, s3, s4
	v_and_b32_e32 v4, 63, v3
	s_addc_u32 s6, s1, s5
	s_ashr_i32 s1, s0, 31
	v_lshrrev_b32_e32 v12, 5, v4
	v_bfe_u32 v13, v3, 1, 2
	s_lshl_b64 s[4:5], s[0:1], 2
	v_lshl_or_b32 v10, v10, 1, v12
	v_bfe_u32 v12, v3, 3, 2
	v_and_b32_e32 v14, 1, v3
	v_lshlrev_b32_e32 v15, 5, v13
	s_add_u32 s24, s3, s4
	v_lshl_or_b32 v15, v12, 7, v15
	v_lshlrev_b32_e32 v16, 16, v10
	v_lshlrev_b32_e32 v17, 4, v14
	s_addc_u32 s1, s6, s5
	v_or3_b32 v225, v15, v17, v16
	s_and_b32 s25, s1, 0xffff
	s_movk_i32 s1, 0x2000
	buffer_load_dwordx4 v[114:117], v225, s[24:27], 0 offen
	buffer_load_dwordx4 v[118:121], v225, s[24:27], s66 offen
	s_mov_b32 s3, 0x8000
	buffer_load_dwordx4 v[126:129], v225, s[24:27], s1 offen
	buffer_load_dwordx4 v[122:125], v225, s[24:27], s3 offen
	s_movk_i32 s1, 0x4000
	s_mov_b32 s3, 0xa000
	buffer_load_dwordx4 v[130:133], v225, s[24:27], s1 offen
	buffer_load_dwordx4 v[134:137], v225, s[24:27], s3 offen
	s_mov_b32 s1, 0xc000
	s_mov_b32 s3, 0xe000
	buffer_load_dwordx4 v[142:145], v225, s[24:27], s1 offen
	buffer_load_dwordx4 v[146:149], v225, s[24:27], s3 offen
	s_waitcnt vmcnt(8)
	v_lshlrev_b32_e32 v7, 10, v7
	v_and_b32_e32 v7, 0xfffff000, v7
	v_lshlrev_b32_e32 v6, 10, v6
	v_and_b32_e32 v6, 0xfffff000, v6
	v_lshlrev_b32_e32 v9, 10, v9
	v_and_b32_e32 v9, 0xfffff000, v9
	v_lshlrev_b32_e32 v8, 10, v8
	v_and_b32_e32 v8, 0xfffff000, v8
	v_lshlrev_b32_e32 v17, 4, v3
	v_lshlrev_b32_e32 v15, 6, v11
	v_and_b32_e32 v16, 32, v3
	v_and_b32_e32 v17, 48, v17
	v_bitop3_b32 v15, v17, v15, v16 bitop3:0xde
	v_or_b32_e32 v221, v9, v15
	v_lshlrev_b32_e32 v9, 2, v12
	v_lshlrev_b32_e32 v11, 1, v11
	v_or3_b32 v9, v9, v11, v14
	v_lshlrev_b32_e32 v11, 2, v3
	v_and_b32_e32 v12, 0xfffffc00, v11
	v_lshl_add_u32 v9, v9, 11, v12
	v_lshlrev_b32_e32 v12, 8, v13
	v_lshlrev_b32_e32 v10, 4, v10
	v_and_or_b32 v10, v10, 48, v12
	v_lshlrev_b32_e32 v12, 3, v3
	v_or_b32_e32 v223, v7, v15
	v_and_b32_e32 v7, 15, v3
	v_and_b32_e32 v12, 32, v12
	v_or_b32_e32 v222, v6, v15
	v_ashrrev_i32_e32 v6, 8, v3
	v_bitop3_b32 v219, v9, v10, v12 bitop3:0xf6
	v_lshlrev_b32_e32 v7, 6, v7
	v_and_b32_e32 v3, 48, v3
	v_and_b32_e32 v10, 32, v11
	v_or_b32_e32 v9, v7, v3
	v_bitop3_b32 v3, v7, v10, v3 bitop3:0x36
	v_lshlrev_b32_e32 v11, 13, v5
	v_lshlrev_b32_e32 v220, 6, v14
	v_lshlrev_b32_e32 v4, 4, v4
	v_lshlrev_b32_e32 v7, 14, v6
	v_and_or_b32 v226, v11, s66, v3
	v_cmp_eq_u32_e32 vcc, 0, v215
	v_add_u32_e32 v227, 0, v219
	v_add_u32_e32 v3, 0xc0, v220
	v_or_b32_e32 v224, v8, v15
	v_lshl_or_b32 v229, v5, 10, v4
	v_bitop3_b32 v216, v9, v7, v10 bitop3:0xde
	v_or_b32_e32 v217, 0x8000, v226
	v_readfirstlane_b32 s1, v6
	s_and_b64 vcc, exec, vcc
	v_add_u32_e32 v228, v227, v220
	v_and_b32_e32 v218, 0xc0, v3
	v_readlane_b32 s7, v246, 3
	v_readlane_b32 s8, v246, 4
	v_readlane_b32 s9, v246, 5
	v_readlane_b32 s10, v246, 6
	v_readlane_b32 s11, v246, 7
	s_cbranch_vccnz .LBB0_1263
	s_sub_i32 s3, s87, s2
	s_mov_b32 s99, s3
	v_readfirstlane_b32 s100, v0
	s_nop 3
	s_lshr_b32 s100, s100, 7
	s_lshl_b32 s100, s100, 4
	s_add_i32 s3, s3, 15
	s_ashr_i32 s3, s3, 4
	s_cmp_eq_u32 s1, 0
	s_cselect_b32 s1, s3, 0
	v_readfirstlane_b32 s3, v229
	s_and_b32 s3, s3, 0xfffffc00
	s_add_i32 s3, s3, 0
	s_mov_b32 s38, s26
	s_mov_b32 s39, s27
	s_mov_b32 m0, s3
	s_waitcnt vmcnt(6)
	v_mov_b64_e32 v[4:5], v[118:119]
	buffer_load_dwordx4 v223, s[36:39], 0 offen lds
	s_add_i32 m0, s3, 0x2000
	s_waitcnt vmcnt(3)
	v_mov_b64_e32 v[8:9], v[134:135]
	buffer_load_dwordx4 v222, s[36:39], 0 offen lds
	s_add_i32 m0, s3, 0x4000
	v_mov_b64_e32 v[12:13], v[114:115]
	buffer_load_dwordx4 v221, s[36:39], 0 offen lds
	s_add_i32 m0, s3, 0x6000
	s_waitcnt vmcnt(3)
	v_mov_b64_e32 v[16:17], v[146:147]
	v_mov_b64_e32 v[20:21], v[130:131]
	v_mov_b64_e32 v[24:25], v[122:123]
	v_mov_b64_e32 v[28:29], v[142:143]
	v_mov_b64_e32 v[32:33], v[126:127]
	buffer_load_dwordx4 v224, s[36:39], 0 offen lds
	v_mov_b64_e32 v[6:7], v[120:121]
	v_mov_b64_e32 v[10:11], v[136:137]
	v_mov_b64_e32 v[14:15], v[116:117]
	v_mov_b64_e32 v[18:19], v[148:149]
	v_mov_b64_e32 v[22:23], v[132:133]
	v_mov_b64_e32 v[26:27], v[124:125]
	v_mov_b64_e32 v[30:31], v[144:145]
	v_mov_b64_e32 v[34:35], v[128:129]
	s_waitcnt vmcnt(0)
	s_movk_i32 s101, 0x80
	s_cmp_le_i32 s99, s100
	s_cbranch_scc1 .Lmy_rcgP0
	buffer_load_dwordx4 v[236:239], v223, s[36:39], s101 offen
